# loop-edge edits: SB running ring offset instead of two divisions by six per step; NSA latch enters the lean step directly
# speedup vs baseline: 1.0032x; 1.0032x over previous
.LBB0_515:
	v_ashrrev_i32_e32 v118, 3, v119
	v_lshlrev_b32_e32 v7, 1, v119
	v_lshlrev_b32_e32 v9, 6, v118
	v_and_b32_e32 v7, 32, v7
	v_and_b32_e32 v9, 0xffffff00, v9
	v_and_b32_e32 v4, 0xc0, v4
	v_lshlrev_b32_e32 v8, 3, v119
	v_or3_b32 v4, v9, v4, v7
	v_lshlrev_b32_e32 v5, 4, v163
	v_lshlrev_b32_e32 v6, 2, v3
	v_and_b32_e32 v8, 24, v8
	v_add_u32_e32 v167, 0x2000, v4
	v_add_u32_e32 v167, v167, v8
	v_add_u32_e32 v4, s28, v163
	v_mov_b32_e32 v16, v2
	v_mov_b32_e32 v17, v2
	v_sub_u32_e32 v166, v163, v6
	v_sub_u32_e32 v184, v4, v6
	v_lshl_or_b32 v185, v3, 10, v5
	v_cmp_gt_i32_e32 vcc, 0, v166
	s_nop 1
	v_cndmask_b32_e32 v5, 0, v162, vcc
	v_cmp_lt_i32_e32 vcc, 0, v166
	s_nop 1
	v_cndmask_b32_e64 v6, 1.0, 0, vcc
	v_or_b32_e32 v172, v5, v6
	v_cmp_gt_i32_e32 vcc, 2, v166
	s_nop 1
	v_cndmask_b32_e32 v5, 0, v162, vcc
	v_cmp_lt_i32_e32 vcc, 2, v166
	s_nop 1
	v_cndmask_b32_e64 v6, 1.0, 0, vcc
	v_or_b32_e32 v173, v5, v6
	v_cmp_gt_i32_e32 vcc, 8, v166
	s_nop 1
	v_cndmask_b32_e32 v5, 0, v162, vcc
	v_cmp_lt_i32_e32 vcc, 8, v166
	s_nop 1
	v_cndmask_b32_e64 v6, 1.0, 0, vcc
	v_or_b32_e32 v174, v5, v6
	v_cmp_gt_i32_e32 vcc, 10, v166
	s_nop 1
	v_cndmask_b32_e32 v5, 0, v162, vcc
	v_cmp_lt_i32_e32 vcc, 10, v166
	s_nop 1
	v_cndmask_b32_e64 v6, 1.0, 0, vcc
	v_or_b32_e32 v175, v5, v6
	v_cmp_gt_i32_e32 vcc, 16, v166
	s_nop 1
	v_cndmask_b32_e32 v5, 0, v162, vcc
	v_cmp_lt_i32_e32 vcc, 16, v166
	s_nop 1
	v_cndmask_b32_e64 v6, 1.0, 0, vcc
	v_or_b32_e32 v176, v5, v6
	v_cmp_gt_i32_e32 vcc, 18, v166
	s_nop 1
	v_cndmask_b32_e32 v5, 0, v162, vcc
	v_cmp_lt_i32_e32 vcc, 18, v166
	s_nop 1
	v_cndmask_b32_e64 v6, 1.0, 0, vcc
	v_or_b32_e32 v177, v5, v6
	v_cmp_gt_i32_e32 vcc, 24, v166
	s_nop 1
	v_cndmask_b32_e32 v5, 0, v162, vcc
	v_cmp_lt_i32_e32 vcc, 24, v166
	s_nop 1
	v_cndmask_b32_e64 v6, 1.0, 0, vcc
	v_or_b32_e32 v178, v5, v6
	v_cmp_gt_i32_e32 vcc, 26, v166
	s_nop 1
	v_cndmask_b32_e32 v5, 0, v162, vcc
	v_cmp_lt_i32_e32 vcc, 26, v166
	s_nop 1
	v_cndmask_b32_e64 v6, 1.0, 0, vcc
	v_or_b32_e32 v179, v5, v6
	v_mov_b32_e32 v180, 0x3f803f80
	v_mov_b32_e32 v181, 0x3f803f80
	v_mov_b32_e32 v182, 0x3f803f80
	v_mov_b32_e32 v183, 0x3f803f80
	v_mov_b32_e32 v3, v2
	v_mov_b32_e32 v4, v2
	v_mov_b32_e32 v5, v2
	v_mov_b32_e32 v6, v2
	v_mov_b32_e32 v7, v2
	v_mov_b32_e32 v8, v2
	v_mov_b32_e32 v9, v2
	v_mov_b32_e32 v10, v2
	v_mov_b32_e32 v11, v2
	v_mov_b32_e32 v12, v2
	v_mov_b32_e32 v13, v2
	v_mov_b32_e32 v14, v2
	v_mov_b32_e32 v15, v2
	v_mov_b64_e32 v[34:35], v[16:17]
	v_and_b32_e32 v164, 7, v119
	s_lshl_b32 s4, s4, 8
	v_mov_b64_e32 v[32:33], v[14:15]
	v_mov_b64_e32 v[30:31], v[12:13]
	v_mov_b64_e32 v[28:29], v[10:11]
	v_mov_b64_e32 v[26:27], v[8:9]
	v_mov_b64_e32 v[24:25], v[6:7]
	v_mov_b64_e32 v[22:23], v[4:5]
	v_mov_b64_e32 v[20:21], v[2:3]
	v_mov_b64_e32 v[18:19], v[16:17]
	s_add_i32 s16, s3, -2
	s_or_b32 s37, s34, 30
	v_lshl_add_u32 v165, v164, 2, s31
	s_mov_b32 s38, 4
	s_mov_b32 s39, 0
	v_cmp_eq_u32_e64 s[2:3], 0, v119
	s_sub_i32 s40, s5, 31
	s_sub_i32 s41, 0x7c0, s4
	s_sub_i32 s42, 31, s5
	s_mov_b64 s[4:5], 0
	v_mov_b32_e32 v36, 0
	s_mov_b32 s43, 5
	s_mov_b32 s98, 0
	s_mov_b32 s45, 0
	v_mov_b64_e32 v[16:17], v[14:15]
	v_mov_b64_e32 v[14:15], v[12:13]
	v_mov_b64_e32 v[12:13], v[10:11]
	v_mov_b64_e32 v[10:11], v[8:9]
	v_mov_b64_e32 v[8:9], v[6:7]
	v_mov_b64_e32 v[6:7], v[4:5]
	v_mov_b64_e32 v[4:5], v[2:3]
	s_branch .LBB0_518

.LBB0_517:
	s_add_i32 s98, s98, 0x4000
	s_cmp_eq_u32 s98, 0x18000
	s_cselect_b32 s98, 0, s98
	s_add_i32 s17, s40, s43
	s_cmp_eq_u32 s17, 5
	s_cselect_b64 s[48:49], -1, 0
	s_or_b64 s[18:19], s[18:19], s[48:49]
	s_add_i32 s45, s45, 8
	s_add_i32 s16, s16, -1
	s_add_i32 s43, s43, 1
	s_sub_i32 s41, s41, 64
	v_add_u32_e32 v184, 64, v184
	s_add_i32 s38, s38, 1
	s_andn2_b64 vcc, exec, s[18:19]
	s_add_i32 s39, s39, -1
	s_cbranch_vccz .LBB0_502

.LBB0_536:
	s_cmp_ge_u32 s43, s36
	s_cbranch_scc1 .LBB0_538
	s_add_i32 s47, s98, s29
	s_cmp_ge_u32 s98, 0x4000
	s_cselect_b32 s17, 0x18000, 0
	s_sub_i32 m0, s47, s17
	s_ashr_i32 s17, s16, 31
	s_lshl_b64 s[18:19], s[16:17], 13
	v_lshl_add_u64 v[38:39], v[120:121], 0, s[18:19]
	v_lshl_add_u64 v[86:87], v[122:123], 0, s[18:19]
	global_load_lds_dwordx4 v[38:39], off
	s_add_i32 m0, m0, 0x2000
	s_nop 0
	global_load_lds_dwordx4 v[86:87], off
.LBB0_538:
	s_and_b64 vcc, exec, s[4:5]
	s_mov_b64 s[4:5], -1
	s_cbranch_vccnz .LBB0_545
	s_cmp_gt_i32 s41, s37
	s_mov_b64 s[4:5], 0
	s_cbranch_scc1 .LBB0_545
	v_add_u32_e32 v3, s98, v185
	ds_read_b128 v[38:41], v3
	ds_read_b128 v[42:45], v3 offset:512
	ds_read_b128 v[86:89], v3 offset:2048
	ds_read_b128 v[90:93], v3 offset:2560
	s_add_i32 s18, s41, 63
	s_waitcnt lgkmcnt(3)
	v_mfma_f32_32x32x16_bf16 v[54:69], v[38:41], v[82:85], 0
	s_mov_b64 s[4:5], -1
	s_cmp_lt_i32 s18, s34
	s_waitcnt lgkmcnt(2)
	v_mfma_f32_32x32x16_bf16 v[38:53], v[42:45], v[82:85], 0
	s_waitcnt lgkmcnt(1)
	v_mfma_f32_32x32x16_bf16 v[54:69], v[86:89], v[78:81], v[54:69]
	s_waitcnt lgkmcnt(0)
	v_mfma_f32_32x32x16_bf16 v[38:53], v[90:93], v[78:81], v[38:53]
	ds_read_b128 v[86:89], v3 offset:4096
	ds_read_b128 v[90:93], v3 offset:4608
	s_waitcnt lgkmcnt(1)
	v_mfma_f32_32x32x16_bf16 v[54:69], v[86:89], v[74:77], v[54:69]
	s_waitcnt lgkmcnt(0)
	v_mfma_f32_32x32x16_bf16 v[38:53], v[90:93], v[74:77], v[38:53]
	ds_read_b128 v[86:89], v3 offset:6144
	ds_read_b128 v[90:93], v3 offset:6656
	s_waitcnt lgkmcnt(1)
	v_mfma_f32_32x32x16_bf16 v[54:69], v[86:89], v[70:73], v[54:69]
	s_waitcnt lgkmcnt(0)
	v_mfma_f32_32x32x16_bf16 v[38:53], v[90:93], v[70:73], v[38:53]
	s_nop 9
	v_exp_f32_e64 v247, -|v54|
	v_exp_f32_e64 v246, -|v55|
	v_exp_f32_e64 v239, -|v56|
	v_exp_f32_e64 v238, -|v57|
	v_exp_f32_e64 v231, -|v58|
	v_exp_f32_e64 v230, -|v59|
	v_exp_f32_e64 v223, -|v60|
	v_exp_f32_e64 v243, -|v38|
	v_exp_f32_e64 v242, -|v39|
	v_exp_f32_e64 v235, -|v40|
	v_exp_f32_e64 v234, -|v41|
	v_exp_f32_e64 v227, -|v42|
	v_exp_f32_e64 v226, -|v43|
	v_exp_f32_e64 v222, -|v61|
	v_exp_f32_e64 v219, -|v44|
	v_exp_f32_e64 v218, -|v45|
	v_exp_f32_e64 v215, -|v62|
	v_exp_f32_e64 v213, -|v63|
	v_exp_f32_e64 v211, -|v46|
	v_exp_f32_e64 v210, -|v47|
	v_exp_f32_e64 v207, -|v64|
	v_exp_f32_e64 v206, -|v65|
	v_exp_f32_e64 v203, -|v48|
	v_exp_f32_e64 v202, -|v49|
	v_exp_f32_e64 v199, -|v66|
	v_exp_f32_e64 v198, -|v67|
	v_exp_f32_e64 v195, -|v50|
	v_exp_f32_e64 v194, -|v51|
	v_exp_f32_e64 v190, -|v68|
	v_exp_f32_e64 v189, -|v69|
	v_exp_f32_e64 v187, -|v52|
	v_exp_f32_e64 v186, -|v53|
	s_cbranch_scc1 .LBB0_542
	v_add_f32_e32 v86, 1.0, v247
	v_add_f32_e32 v87, 1.0, v246
	v_log_f32_e32 v86, v86
	v_log_f32_e32 v87, v87
	v_max_f32_e32 v88, 0, v54
	v_max_f32_e32 v89, 0, v55
	v_cmp_lt_i32_e32 vcc, 0, v184
	v_pk_add_f32 v[86:87], v[88:89], v[86:87]
	v_cmp_lt_i32_e64 s[4:5], 1, v184
	v_pk_add_f32 v[88:89], v[54:55], v[86:87] neg_lo:[0,1] neg_hi:[0,1]
	v_cndmask_b32_e32 v86, 0, v86, vcc
	v_cndmask_b32_e64 v87, 0, v87, s[4:5]
	v_and_b32_e32 v91, 0xffff0000, v87
	v_and_b32_e32 v90, 0xffff0000, v86
	v_cndmask_b32_e32 v124, v161, v88, vcc
	v_cndmask_b32_e64 v125, v161, v89, s[4:5]
	v_pk_add_f32 v[88:89], v[86:87], 0 op_sel_hi:[1,0]
	v_or_b32_sdwa v98, v91, v86 dst_sel:DWORD dst_unused:UNUSED_PAD src0_sel:DWORD src1_sel:WORD_1
	v_pk_add_f32 v[86:87], v[86:87], v[90:91] neg_lo:[0,1] neg_hi:[0,1]
	v_add_f32_e32 v90, 1.0, v243
	v_add_f32_e32 v91, 1.0, v242
	v_log_f32_e32 v90, v90
	v_log_f32_e32 v91, v91
	v_cvt_pk_bf16_f32 v94, v86, v87
	v_max_f32_e32 v86, 0, v38
	v_max_f32_e32 v87, 0, v39
	v_pk_add_f32 v[86:87], v[86:87], v[90:91]
	v_cmp_lt_i32_e32 vcc, 32, v184
	v_pk_add_f32 v[90:91], v[38:39], v[86:87] neg_lo:[0,1] neg_hi:[0,1]
	v_cmp_lt_i32_e64 s[4:5], 33, v184
	v_cndmask_b32_e32 v126, v161, v90, vcc
	v_cndmask_b32_e32 v90, 0, v86, vcc
	v_cndmask_b32_e64 v127, v161, v91, s[4:5]
	v_cndmask_b32_e64 v91, 0, v87, s[4:5]
	v_and_b32_e32 v93, 0xffff0000, v91
	v_and_b32_e32 v92, 0xffff0000, v90
	v_add_f32_e32 v87, 1.0, v239
	v_pk_add_f32 v[88:89], v[90:91], v[88:89]
	v_or_b32_sdwa v86, v93, v90 dst_sel:DWORD dst_unused:UNUSED_PAD src0_sel:DWORD src1_sel:WORD_1
	v_pk_add_f32 v[90:91], v[90:91], v[92:93] neg_lo:[0,1] neg_hi:[0,1]
	v_log_f32_e32 v92, v87
	v_add_f32_e32 v87, 1.0, v238
	v_log_f32_e32 v93, v87
	v_max_f32_e32 v96, 0, v56
	v_max_f32_e32 v97, 0, v57
	v_cmp_lt_i32_e32 vcc, 2, v184
	v_pk_add_f32 v[92:93], v[96:97], v[92:93]
	v_cmp_lt_i32_e64 s[4:5], 3, v184
	v_pk_add_f32 v[96:97], v[56:57], v[92:93] neg_lo:[0,1] neg_hi:[0,1]
	v_cndmask_b32_e32 v92, 0, v92, vcc
	v_cndmask_b32_e64 v93, 0, v93, s[4:5]
	v_cndmask_b32_e32 v128, v161, v96, vcc
	v_cndmask_b32_e64 v129, v161, v97, s[4:5]
	v_and_b32_e32 v97, 0xffff0000, v93
	v_and_b32_e32 v96, 0xffff0000, v92
	v_add_f32_e32 v87, 1.0, v235
	v_pk_add_f32 v[88:89], v[92:93], v[88:89]
	v_or_b32_sdwa v99, v97, v92 dst_sel:DWORD dst_unused:UNUSED_PAD src0_sel:DWORD src1_sel:WORD_1
	v_pk_add_f32 v[92:93], v[92:93], v[96:97] neg_lo:[0,1] neg_hi:[0,1]
	v_log_f32_e32 v96, v87
	v_add_f32_e32 v87, 1.0, v234
	v_log_f32_e32 v97, v87
	v_cvt_pk_bf16_f32 v95, v92, v93
	v_max_f32_e32 v92, 0, v40
	v_max_f32_e32 v93, 0, v41
	v_pk_add_f32 v[92:93], v[92:93], v[96:97]
	v_cmp_lt_i32_e32 vcc, 34, v184
	v_cmp_lt_i32_e64 s[4:5], 35, v184
	v_pk_add_f32 v[96:97], v[40:41], v[92:93] neg_lo:[0,1] neg_hi:[0,1]
	v_cndmask_b32_e32 v92, 0, v92, vcc
	v_cndmask_b32_e64 v93, 0, v93, s[4:5]
	v_cvt_pk_bf16_f32 v90, v90, v91
	v_cndmask_b32_e32 v130, v161, v96, vcc
	v_cndmask_b32_e64 v131, v161, v97, s[4:5]
	v_and_b32_e32 v97, 0xffff0000, v93
	v_and_b32_e32 v96, 0xffff0000, v92
	v_add_f32_e32 v91, 1.0, v231
	v_pk_add_f32 v[88:89], v[92:93], v[88:89]
	v_or_b32_sdwa v87, v97, v92 dst_sel:DWORD dst_unused:UNUSED_PAD src0_sel:DWORD src1_sel:WORD_1
	v_pk_add_f32 v[92:93], v[92:93], v[96:97] neg_lo:[0,1] neg_hi:[0,1]
	v_log_f32_e32 v96, v91
	v_add_f32_e32 v91, 1.0, v230
	v_log_f32_e32 v97, v91
	v_cvt_pk_bf16_f32 v91, v92, v93
	v_max_f32_e32 v92, 0, v58
	v_max_f32_e32 v93, 0, v59
	v_pk_add_f32 v[92:93], v[92:93], v[96:97]
	v_cmp_lt_i32_e32 vcc, 8, v184
	v_cmp_lt_i32_e64 s[4:5], 9, v184
	v_pk_add_f32 v[96:97], v[58:59], v[92:93] neg_lo:[0,1] neg_hi:[0,1]
	v_cndmask_b32_e32 v92, 0, v92, vcc
	v_cndmask_b32_e64 v93, 0, v93, s[4:5]
	v_cndmask_b32_e32 v132, v161, v96, vcc
	v_cndmask_b32_e64 v133, v161, v97, s[4:5]
	v_and_b32_e32 v97, 0xffff0000, v93
	v_and_b32_e32 v96, 0xffff0000, v92
	v_pk_add_f32 v[88:89], v[92:93], v[88:89]
	v_or_b32_sdwa v100, v97, v92 dst_sel:DWORD dst_unused:UNUSED_PAD src0_sel:DWORD src1_sel:WORD_1
	v_pk_add_f32 v[92:93], v[92:93], v[96:97] neg_lo:[0,1] neg_hi:[0,1]
	v_add_f32_e32 v96, 1.0, v227
	v_log_f32_e32 v102, v96
	v_add_f32_e32 v96, 1.0, v226
	v_log_f32_e32 v103, v96
	v_cvt_pk_bf16_f32 v96, v92, v93
	v_max_f32_e32 v92, 0, v42
	v_max_f32_e32 v93, 0, v43
	v_pk_add_f32 v[92:93], v[92:93], v[102:103]
	v_cmp_lt_i32_e32 vcc, 40, v184
	v_cmp_lt_i32_e64 s[4:5], 41, v184
	v_pk_add_f32 v[102:103], v[42:43], v[92:93] neg_lo:[0,1] neg_hi:[0,1]
	v_cndmask_b32_e32 v92, 0, v92, vcc
	v_cndmask_b32_e64 v93, 0, v93, s[4:5]
	v_cndmask_b32_e32 v134, v161, v102, vcc
	v_cndmask_b32_e64 v135, v161, v103, s[4:5]
	v_pk_add_f32 v[102:103], v[92:93], v[88:89]
	v_and_b32_e32 v105, 0xffff0000, v93
	v_and_b32_e32 v104, 0xffff0000, v92
	v_add_f32_e32 v89, 1.0, v223
	v_or_b32_sdwa v88, v105, v92 dst_sel:DWORD dst_unused:UNUSED_PAD src0_sel:DWORD src1_sel:WORD_1
	v_pk_add_f32 v[92:93], v[92:93], v[104:105] neg_lo:[0,1] neg_hi:[0,1]
	v_log_f32_e32 v104, v89
	v_add_f32_e32 v89, 1.0, v222
	v_log_f32_e32 v105, v89
	v_max_f32_e32 v106, 0, v60
	v_max_f32_e32 v107, 0, v61
	v_cmp_lt_i32_e32 vcc, 10, v184
	v_pk_add_f32 v[104:105], v[106:107], v[104:105]
	v_cmp_lt_i32_e64 s[4:5], 11, v184
	v_pk_add_f32 v[106:107], v[60:61], v[104:105] neg_lo:[0,1] neg_hi:[0,1]
	v_cndmask_b32_e32 v104, 0, v104, vcc
	v_cndmask_b32_e64 v105, 0, v105, s[4:5]
	v_cndmask_b32_e32 v136, v161, v106, vcc
	v_cndmask_b32_e64 v137, v161, v107, s[4:5]
	v_and_b32_e32 v107, 0xffff0000, v105
	v_and_b32_e32 v106, 0xffff0000, v104
	v_add_f32_e32 v89, 1.0, v219
	v_pk_add_f32 v[102:103], v[104:105], v[102:103]
	v_or_b32_sdwa v101, v107, v104 dst_sel:DWORD dst_unused:UNUSED_PAD src0_sel:DWORD src1_sel:WORD_1
	v_pk_add_f32 v[104:105], v[104:105], v[106:107] neg_lo:[0,1] neg_hi:[0,1]
	v_log_f32_e32 v106, v89
	v_add_f32_e32 v89, 1.0, v218
	v_log_f32_e32 v107, v89
	v_cvt_pk_bf16_f32 v97, v104, v105
	v_max_f32_e32 v104, 0, v44
	v_max_f32_e32 v105, 0, v45
	v_pk_add_f32 v[104:105], v[104:105], v[106:107]
	v_cmp_lt_i32_e32 vcc, 42, v184
	v_cmp_lt_i32_e64 s[4:5], 43, v184
	v_pk_add_f32 v[106:107], v[44:45], v[104:105] neg_lo:[0,1] neg_hi:[0,1]
	v_cndmask_b32_e32 v104, 0, v104, vcc
	v_cndmask_b32_e64 v105, 0, v105, s[4:5]
	v_cvt_pk_bf16_f32 v92, v92, v93
	v_cndmask_b32_e32 v138, v161, v106, vcc
	v_cndmask_b32_e64 v139, v161, v107, s[4:5]
	v_and_b32_e32 v107, 0xffff0000, v105
	v_and_b32_e32 v106, 0xffff0000, v104
	v_add_f32_e32 v93, 1.0, v215
	v_pk_add_f32 v[102:103], v[104:105], v[102:103]
	v_or_b32_sdwa v89, v107, v104 dst_sel:DWORD dst_unused:UNUSED_PAD src0_sel:DWORD src1_sel:WORD_1
	v_pk_add_f32 v[104:105], v[104:105], v[106:107] neg_lo:[0,1] neg_hi:[0,1]
	v_log_f32_e32 v106, v93
	v_add_f32_e32 v93, 1.0, v213
	v_log_f32_e32 v107, v93
	v_cvt_pk_bf16_f32 v93, v104, v105
	v_max_f32_e32 v104, 0, v62
	v_max_f32_e32 v105, 0, v63
	v_pk_add_f32 v[104:105], v[104:105], v[106:107]
	v_cmp_lt_i32_e32 vcc, 16, v184
	v_cmp_lt_i32_e64 s[4:5], 17, v184
	v_pk_add_f32 v[106:107], v[62:63], v[104:105] neg_lo:[0,1] neg_hi:[0,1]
	v_cndmask_b32_e32 v104, 0, v104, vcc
	v_cndmask_b32_e64 v105, 0, v105, s[4:5]
	v_cndmask_b32_e32 v140, v161, v106, vcc
	v_cndmask_b32_e64 v141, v161, v107, s[4:5]
	v_and_b32_e32 v107, 0xffff0000, v105
	v_and_b32_e32 v106, 0xffff0000, v104
	v_pk_add_f32 v[102:103], v[104:105], v[102:103]
	v_or_b32_sdwa v110, v107, v104 dst_sel:DWORD dst_unused:UNUSED_PAD src0_sel:DWORD src1_sel:WORD_1
	v_pk_add_f32 v[104:105], v[104:105], v[106:107] neg_lo:[0,1] neg_hi:[0,1]
	v_add_f32_e32 v106, 1.0, v211
	v_add_f32_e32 v107, 1.0, v210
	v_log_f32_e32 v106, v106
	v_log_f32_e32 v107, v107
	v_cvt_pk_bf16_f32 v114, v104, v105
	v_max_f32_e32 v104, 0, v46
	v_max_f32_e32 v105, 0, v47
	v_pk_add_f32 v[104:105], v[104:105], v[106:107]
	v_cmp_lt_i32_e32 vcc, 48, v184
	v_cmp_lt_i32_e64 s[4:5], 49, v184
	v_pk_add_f32 v[106:107], v[46:47], v[104:105] neg_lo:[0,1] neg_hi:[0,1]
	v_cndmask_b32_e32 v104, 0, v104, vcc
	v_cndmask_b32_e64 v105, 0, v105, s[4:5]
	v_pk_add_f32 v[108:109], v[104:105], v[102:103]
	v_and_b32_e32 v103, 0xffff0000, v105
	v_and_b32_e32 v102, 0xffff0000, v104
	v_cndmask_b32_e32 v144, v161, v106, vcc
	v_or_b32_sdwa v106, v103, v104 dst_sel:DWORD dst_unused:UNUSED_PAD src0_sel:DWORD src1_sel:WORD_1
	v_pk_add_f32 v[102:103], v[104:105], v[102:103] neg_lo:[0,1] neg_hi:[0,1]
	v_add_f32_e32 v104, 1.0, v207
	v_add_f32_e32 v105, 1.0, v206
	v_log_f32_e32 v104, v104
	v_log_f32_e32 v105, v105
	v_max_f32_e32 v112, 0, v64
	v_max_f32_e32 v113, 0, v65
	v_cndmask_b32_e64 v145, v161, v107, s[4:5]
	v_pk_add_f32 v[104:105], v[112:113], v[104:105]
	v_cmp_lt_i32_e32 vcc, 18, v184
	v_cmp_lt_i32_e64 s[4:5], 19, v184
	v_pk_add_f32 v[112:113], v[64:65], v[104:105] neg_lo:[0,1] neg_hi:[0,1]
	v_cndmask_b32_e32 v104, 0, v104, vcc
	v_cndmask_b32_e64 v105, 0, v105, s[4:5]
	v_cvt_pk_bf16_f32 v102, v102, v103
	v_cndmask_b32_e32 v146, v161, v112, vcc
	v_cndmask_b32_e64 v147, v161, v113, s[4:5]
	v_and_b32_e32 v113, 0xffff0000, v105
	v_and_b32_e32 v112, 0xffff0000, v104
	v_add_f32_e32 v103, 1.0, v203
	v_pk_add_f32 v[108:109], v[104:105], v[108:109]
	v_or_b32_sdwa v111, v113, v104 dst_sel:DWORD dst_unused:UNUSED_PAD src0_sel:DWORD src1_sel:WORD_1
	v_pk_add_f32 v[104:105], v[104:105], v[112:113] neg_lo:[0,1] neg_hi:[0,1]
	v_log_f32_e32 v112, v103
	v_add_f32_e32 v103, 1.0, v202
	v_log_f32_e32 v113, v103
	v_cvt_pk_bf16_f32 v115, v104, v105
	v_max_f32_e32 v104, 0, v48
	v_max_f32_e32 v105, 0, v49
	v_pk_add_f32 v[104:105], v[104:105], v[112:113]
	v_cmp_lt_i32_e32 vcc, 50, v184
	v_cmp_lt_i32_e64 s[4:5], 51, v184
	v_pk_add_f32 v[112:113], v[48:49], v[104:105] neg_lo:[0,1] neg_hi:[0,1]
	v_cndmask_b32_e32 v104, 0, v104, vcc
	v_cndmask_b32_e64 v105, 0, v105, s[4:5]
	v_cndmask_b32_e32 v152, v161, v112, vcc
	v_cndmask_b32_e64 v153, v161, v113, s[4:5]
	v_and_b32_e32 v113, 0xffff0000, v105
	v_and_b32_e32 v112, 0xffff0000, v104
	v_add_f32_e32 v103, 1.0, v199
	v_pk_add_f32 v[108:109], v[104:105], v[108:109]
	v_or_b32_sdwa v107, v113, v104 dst_sel:DWORD dst_unused:UNUSED_PAD src0_sel:DWORD src1_sel:WORD_1
	v_pk_add_f32 v[104:105], v[104:105], v[112:113] neg_lo:[0,1] neg_hi:[0,1]
	v_log_f32_e32 v112, v103
	v_add_f32_e32 v103, 1.0, v198
	v_log_f32_e32 v113, v103
	v_cvt_pk_bf16_f32 v103, v104, v105
	v_max_f32_e32 v104, 0, v66
	v_max_f32_e32 v105, 0, v67
	v_pk_add_f32 v[104:105], v[104:105], v[112:113]
	v_cmp_lt_i32_e64 s[4:5], 25, v184
	v_pk_add_f32 v[112:113], v[66:67], v[104:105] neg_lo:[0,1] neg_hi:[0,1]
	v_cmp_lt_i32_e32 vcc, 24, v184
	v_cndmask_b32_e64 v157, v161, v113, s[4:5]
	v_add_f32_e32 v113, 1.0, v195
	v_log_f32_e32 v142, v113
	v_add_f32_e32 v113, 1.0, v194
	v_cndmask_b32_e64 v105, 0, v105, s[4:5]
	v_cndmask_b32_e32 v104, 0, v104, vcc
	v_log_f32_e32 v143, v113
	v_and_b32_e32 v117, 0xffff0000, v105
	v_and_b32_e32 v116, 0xffff0000, v104
	v_cndmask_b32_e32 v156, v161, v112, vcc
	v_pk_add_f32 v[108:109], v[104:105], v[108:109]
	v_or_b32_sdwa v112, v117, v104 dst_sel:DWORD dst_unused:UNUSED_PAD src0_sel:DWORD src1_sel:WORD_1
	v_pk_add_f32 v[104:105], v[104:105], v[116:117] neg_lo:[0,1] neg_hi:[0,1]
	v_cmp_lt_i32_e32 vcc, 56, v184
	v_cvt_pk_bf16_f32 v116, v104, v105
	v_max_f32_e32 v104, 0, v50
	v_max_f32_e32 v105, 0, v51
	v_pk_add_f32 v[104:105], v[104:105], v[142:143]
	v_cmp_lt_i32_e64 s[4:5], 57, v184
	v_pk_add_f32 v[142:143], v[50:51], v[104:105] neg_lo:[0,1] neg_hi:[0,1]
	v_cndmask_b32_e32 v104, 0, v104, vcc
	v_cndmask_b32_e64 v105, 0, v105, s[4:5]
	v_cndmask_b32_e32 v158, v161, v142, vcc
	v_cndmask_b32_e64 v159, v161, v143, s[4:5]
	v_pk_add_f32 v[142:143], v[104:105], v[108:109]
	v_and_b32_e32 v149, 0xffff0000, v105
	v_and_b32_e32 v148, 0xffff0000, v104
	v_add_f32_e32 v109, 1.0, v190
	v_or_b32_sdwa v108, v149, v104 dst_sel:DWORD dst_unused:UNUSED_PAD src0_sel:DWORD src1_sel:WORD_1
	v_pk_add_f32 v[104:105], v[104:105], v[148:149] neg_lo:[0,1] neg_hi:[0,1]
	v_log_f32_e32 v148, v109
	v_add_f32_e32 v109, 1.0, v189
	v_log_f32_e32 v149, v109
	v_max_f32_e32 v150, 0, v68
	v_max_f32_e32 v151, 0, v69
	v_cmp_lt_i32_e32 vcc, 26, v184
	v_pk_add_f32 v[148:149], v[150:151], v[148:149]
	v_cmp_lt_i32_e64 s[4:5], 27, v184
	v_pk_add_f32 v[150:151], v[68:69], v[148:149] neg_lo:[0,1] neg_hi:[0,1]
	v_cndmask_b32_e32 v148, 0, v148, vcc
	v_cndmask_b32_e64 v149, 0, v149, s[4:5]
	v_cvt_pk_bf16_f32 v104, v104, v105
	v_cndmask_b32_e32 v154, v161, v150, vcc
	v_cndmask_b32_e64 v155, v161, v151, s[4:5]
	v_and_b32_e32 v151, 0xffff0000, v149
	v_and_b32_e32 v150, 0xffff0000, v148
	v_add_f32_e32 v105, 1.0, v187
	v_pk_add_f32 v[142:143], v[148:149], v[142:143]
	v_or_b32_sdwa v113, v151, v148 dst_sel:DWORD dst_unused:UNUSED_PAD src0_sel:DWORD src1_sel:WORD_1
	v_pk_add_f32 v[148:149], v[148:149], v[150:151] neg_lo:[0,1] neg_hi:[0,1]
	v_log_f32_e32 v150, v105
	v_add_f32_e32 v105, 1.0, v186
	v_log_f32_e32 v151, v105
	v_cvt_pk_bf16_f32 v117, v148, v149
	v_max_f32_e32 v148, 0, v52
	v_max_f32_e32 v149, 0, v53
	v_pk_add_f32 v[148:149], v[148:149], v[150:151]
	v_cmp_lt_i32_e32 vcc, 58, v184
	v_pk_add_f32 v[150:151], v[52:53], v[148:149] neg_lo:[0,1] neg_hi:[0,1]
	v_cmp_lt_i32_e64 s[4:5], 59, v184
	v_cndmask_b32_e32 v150, v161, v150, vcc
	v_cndmask_b32_e32 v148, 0, v148, vcc
	v_cndmask_b32_e64 v151, v161, v151, s[4:5]
	v_cndmask_b32_e64 v149, 0, v149, s[4:5]
	s_mov_b64 s[4:5], 0

.LBB0_544:
	s_mov_b32 s4, 0x43000000
	v_mov_b32_e32 v37, v36
	v_mov_b32_e32 v38, v36
	v_mov_b32_e32 v39, v36
	v_mov_b32_e32 v40, v36
	v_mov_b32_e32 v41, v36
	v_mov_b32_e32 v42, v36
	v_mov_b32_e32 v43, v36
	v_mov_b32_e32 v44, v36
	v_mov_b32_e32 v45, v36
	v_mov_b32_e32 v46, v36
	v_mov_b32_e32 v47, v36
	v_mov_b32_e32 v48, v36
	v_mov_b32_e32 v49, v36
	v_mov_b32_e32 v50, v36
	v_mov_b32_e32 v51, v36
	v_and_b32_e32 v53, 0xffff0000, v149
	v_and_b32_e32 v52, 0xffff0000, v148
	v_add_u32_e32 v3, s98, v167
	v_mfma_f32_32x32x16_bf16 v[54:69], v[172:175], v[98:101], v[36:51]
	v_or_b32_sdwa v109, v53, v148 dst_sel:DWORD dst_unused:UNUSED_PAD src0_sel:DWORD src1_sel:WORD_1
	v_add_f32_e64 v52, v148, -v52
	v_add_f32_e64 v53, v149, -v53
	v_mfma_f32_32x32x16_bf16 v[200:215], v[172:175], v[86:89], v[36:51]
	v_cvt_pk_bf16_f32 v105, v52, v53
	v_mfma_f32_32x32x16_bf16 v[54:69], v[172:175], v[94:97], v[54:69]
	v_mfma_f32_32x32x16_bf16 v[200:215], v[172:175], v[90:93], v[200:215]
	v_mfma_f32_32x32x16_bf16 v[54:69], v[176:179], v[110:113], v[54:69]
	v_mfma_f32_32x32x16_bf16 v[54:69], v[176:179], v[114:117], v[54:69]
	v_mfma_f32_32x32x16_bf16 v[54:69], v[180:183], v[86:89], v[54:69]
	v_mfma_f32_32x32x16_bf16 v[200:215], v[176:179], v[106:109], v[200:215]
	v_mfma_f32_32x32x16_bf16 v[54:69], v[180:183], v[90:93], v[54:69]
	v_mfma_f32_32x32x16_bf16 v[54:69], v[180:183], v[106:109], v[54:69]
	v_mfma_f32_32x32x16_bf16 v[200:215], v[176:179], v[102:105], v[200:215]
	v_mfma_f32_32x32x16_bf16 v[54:69], v[180:183], v[102:105], v[54:69]
	s_nop 10
	v_sub_f32_e32 v38, v126, v200
	v_exp_f32_e32 v100, v38
	v_sub_f32_e32 v38, v125, v55
	v_exp_f32_e32 v55, v38
	v_sub_f32_e32 v38, v127, v201
	v_exp_f32_e32 v101, v38
	v_sub_f32_e32 v38, v128, v56
	v_exp_f32_e32 v56, v38
	v_sub_f32_e32 v38, v130, v202
	v_exp_f32_e32 v102, v38
	v_sub_f32_e32 v38, v129, v57
	v_exp_f32_e32 v57, v38
	v_sub_f32_e32 v38, v131, v203
	v_exp_f32_e32 v103, v38
	v_sub_f32_e32 v38, v132, v58
	v_exp_f32_e32 v58, v38
	v_sub_f32_e32 v38, v134, v204
	v_exp_f32_e32 v104, v38
	v_sub_f32_e32 v38, v133, v59
	v_exp_f32_e32 v59, v38
	v_sub_f32_e32 v38, v135, v205
	v_exp_f32_e32 v105, v38
	v_sub_f32_e32 v38, v136, v60
	v_exp_f32_e32 v60, v38
	v_sub_f32_e32 v38, v138, v206
	v_exp_f32_e32 v106, v38
	v_sub_f32_e32 v38, v137, v61
	v_exp_f32_e32 v61, v38
	v_sub_f32_e32 v38, v139, v207
	v_exp_f32_e32 v107, v38
	v_sub_f32_e32 v38, v140, v62
	v_exp_f32_e32 v62, v38
	v_sub_f32_e32 v38, v144, v208
	v_exp_f32_e32 v108, v38
	v_sub_f32_e32 v38, v141, v63
	v_exp_f32_e32 v63, v38
	v_sub_f32_e32 v38, v145, v209
	v_exp_f32_e32 v109, v38
	v_sub_f32_e32 v38, v146, v64
	v_exp_f32_e32 v64, v38
	v_sub_f32_e32 v38, v152, v210
	v_exp_f32_e32 v110, v38
	v_sub_f32_e32 v38, v147, v65
	v_exp_f32_e32 v65, v38
	v_sub_f32_e32 v38, v153, v211
	v_exp_f32_e32 v111, v38
	v_sub_f32_e32 v38, v156, v66
	v_exp_f32_e32 v66, v38
	v_sub_f32_e32 v38, v158, v212
	v_exp_f32_e32 v112, v38
	v_sub_f32_e32 v38, v157, v67
	v_exp_f32_e32 v50, v38
	v_sub_f32_e32 v38, v159, v213
	v_exp_f32_e32 v67, v38
	v_sub_f32_e32 v38, v154, v68
	v_sub_f32_e32 v54, v124, v54
	v_exp_f32_e32 v51, v38
	v_exp_f32_e32 v54, v54
	ds_read_b64_tr_b16 v[38:39], v3
	ds_read_b64_tr_b16 v[40:41], v3 offset:512
	ds_read_b64_tr_b16 v[48:49], v3 offset:4608
	ds_read_b64_tr_b16 v[46:47], v3 offset:4096
	v_cvt_pk_bf16_f32 v43, v56, v57
	v_cvt_pk_bf16_f32 v42, v54, v55
	v_cvt_pk_bf16_f32 v44, v58, v59
	v_cvt_pk_bf16_f32 v45, v60, v61
	s_waitcnt lgkmcnt(2)
	s_nop 0
	v_mfma_f32_32x32x16_bf16 v[20:35], v[38:41], v[42:45], v[20:35]
	v_sub_f32_e32 v38, v155, v69
	v_exp_f32_e32 v41, v38
	ds_read_b64_tr_b16 v[54:55], v3 offset:1024
	ds_read_b64_tr_b16 v[56:57], v3 offset:1536
	v_cvt_pk_bf16_f32 v38, v62, v63
	v_cvt_pk_bf16_f32 v39, v64, v65
	s_waitcnt lgkmcnt(2)
	v_mfma_f32_32x32x16_bf16 v[4:19], v[46:49], v[42:45], v[4:19]
	ds_read_b64_tr_b16 v[42:43], v3 offset:5120
	ds_read_b64_tr_b16 v[44:45], v3 offset:5632
	v_cvt_pk_bf16_f32 v40, v66, v50
	v_cvt_pk_bf16_f32 v41, v51, v41
	s_waitcnt lgkmcnt(2)
	v_mfma_f32_32x32x16_bf16 v[20:35], v[54:57], v[38:41], v[20:35]
	ds_read_b64_tr_b16 v[54:55], v3 offset:2048
	ds_read_b64_tr_b16 v[56:57], v3 offset:2560
	v_sub_f32_e32 v46, v150, v214
	v_exp_f32_e32 v58, v46
	v_cvt_pk_bf16_f32 v46, v100, v101
	v_cvt_pk_bf16_f32 v47, v102, v103
	v_cvt_pk_bf16_f32 v48, v104, v105
	v_cvt_pk_bf16_f32 v49, v106, v107
	s_waitcnt lgkmcnt(2)
	v_mfma_f32_32x32x16_bf16 v[4:19], v[42:45], v[38:41], v[4:19]
	ds_read_b64_tr_b16 v[38:39], v3 offset:6144
	ds_read_b64_tr_b16 v[40:41], v3 offset:6656
	v_sub_f32_e32 v42, v151, v215
	v_exp_f32_e32 v45, v42
	s_waitcnt lgkmcnt(2)
	v_mfma_f32_32x32x16_bf16 v[20:35], v[54:57], v[46:49], v[20:35]
	ds_read_b64_tr_b16 v[50:51], v3 offset:3072
	ds_read_b64_tr_b16 v[52:53], v3 offset:3584
	v_cvt_pk_bf16_f32 v42, v108, v109
	v_cvt_pk_bf16_f32 v43, v110, v111
	v_cvt_pk_bf16_f32 v44, v112, v67
	v_cvt_pk_bf16_f32 v45, v58, v45
	s_waitcnt lgkmcnt(2)
	v_mfma_f32_32x32x16_bf16 v[4:19], v[38:41], v[46:49], v[4:19]
	ds_read_b64_tr_b16 v[38:39], v3 offset:7168
	ds_read_b64_tr_b16 v[40:41], v3 offset:7680
	v_add_f32_e64 v46, v148, v142
	v_add_f32_e64 v47, v149, v143
	v_pk_add_f32 v[46:47], v[46:47], v[46:47] op_sel:[0,1] op_sel_hi:[1,0]
	s_nop 0
	v_mov_b32_e32 v3, v46
	s_nop 1
	v_permlane32_swap_b32_e32 v46, v3
	s_waitcnt lgkmcnt(2)
	v_mfma_f32_32x32x16_bf16 v[20:35], v[50:53], v[42:45], v[20:35]
	v_add_f32_e32 v3, v46, v3
	v_add_f32_e32 v36, v36, v3
	v_cmp_lt_f32_e32 vcc, s4, v36
	s_cmp_eq_u64 vcc, exec
	s_cselect_b64 s[4:5], -1, 0
	s_waitcnt lgkmcnt(0)
	v_mfma_f32_32x32x16_bf16 v[4:19], v[38:41], v[42:45], v[4:19]

.Lnsa_step_lean:
	s_waitcnt vmcnt(8) lgkmcnt(0)
	s_barrier
	s_mov_b64 s[86:87], 0
	v_lshl_add_u64 v[4:5], s[100:101], 0, v[184:185]
	s_sub_i32 s3, s32, 0x4000
	s_cmp_lt_i32 s3, 0
	s_cselect_b32 s3, 0x14000, s3
	s_mov_b64 s[0:1], 0x800000
	s_add_i32 m0, s98, s3
	s_add_u32 s100, s100, 0x2000
	s_addc_u32 s101, s101, 0
	global_load_lds_dwordx4 v[4:5], off
	v_lshl_add_u64 v[4:5], v[4:5], 0, s[0:1]
	s_add_i32 m0, m0, 0x2000
	s_add_i32 s0, s2, 5
	s_cmp_lg_u32 s0, s80
	global_load_lds_dwordx4 v[4:5], off
	s_cbranch_scc1 .LBB0_599
	v_readlane_b32 s100, v251, 59
	v_readlane_b32 s101, v251, 61
	s_add_u32 s100, s100, s90
	s_addc_u32 s101, s101, s91
	s_branch .LBB0_599

.LBB0_626:
	s_add_i32 s0, s2, 1
	s_cmp_eq_u32 s2, s83
	s_cbranch_scc1 .LBB0_558
	s_add_i32 s32, s32, 0x4000
	s_cmp_eq_u32 s32, 0x18000
	s_cselect_b32 s32, 0, s32
	s_cmp_lt_u32 s2, s99
	s_mov_b32 s2, s0
	s_cbranch_scc1 .Lnsa_step_lean
	s_branch .Lnsa_step_general
